# P2 attention: per-head sink logit fetched with a scalar load (s_load_dword + lgkmcnt) instead of a vector load followed by a full vmcnt(0) drain at every sub-block start
# speedup vs baseline: 1.0083x; 1.0078x over previous
.LBB0_306:
	s_mul_i32 s12, s22, s55
	s_sub_i32 s14, s7, s12
	s_and_b64 s[12:13], s[86:87], exec
	s_cselect_b32 s50, s14, 0
	s_andn2_b64 vcc, exec, s[0:1]
	s_cbranch_vccnz .LBB0_308
	s_ashr_i32 s51, s50, 31
	s_lshl_b64 s[12:13], s[50:51], 2
	s_add_u32 s12, s44, s12
	s_addc_u32 s13, s45, s13
	s_load_dword s14, s[12:13], 0x0
	s_waitcnt lgkmcnt(0)
	s_mov_b32 s12, 1.0
	v_mov_b32_e32 v3, s14
	v_mul_f32_e32 v205, 0x3fb8aa3b, v3
	s_branch .LBB0_309
